# adds MoE unit scheduler: row block by shift (was 64-bit software division), expert lookup = one lane-parallel LDS read + compare + popcount (was 16 dependent LDS round trips)
# speedup vs baseline: 1.0115x; 1.0066x over previous
.LBB0_1893:
	s_andn2_b64 vcc, exec, s[38:39]
	s_mov_b64 s[42:43], 0
	s_cbranch_vccnz .LBB0_1898
	s_sub_i32 s28, 3, s3
	s_lshr_b32 s28, s0, s28
.LBB0_1897:
	v_readlane_b32 s1, v254, 51
	s_mov_b64 s[42:43], -1
	s_mov_b32 s88, s3
	v_and_b32_e32 v5, 63, v0
	s_nop 0
	v_lshl_add_u32 v4, v5, 2, s1
	ds_read_b32 v4, v4
	s_waitcnt lgkmcnt(0)
	v_cmp_ge_i32_e64 s[100:101], s28, v4
	s_nop 3
	s_and_b32 s100, s100, 0x7fffffff
	s_bcnt1_i32_b32 s1, s100
	s_lshl_b32 s29, s1, 2
	s_add_i32 s29, s29, 0
	s_add_i32 s29, s29, 0x23400
	v_mov_b32_e32 v4, s29
	ds_read_b32 v4, v4
	s_lshl_b32 s30, s1, 6
	s_waitcnt lgkmcnt(0)
	v_sub_u32_e32 v4, s28, v4
	s_nop 0
	v_readfirstlane_b32 s29, v4
	s_add_i32 s30, s29, s30
	s_mul_i32 s29, s28, s2
	s_sub_i32 s29, s0, s29
	s_mul_i32 s0, s1, s2
	s_add_i32 s34, s0, s29
